# v7 + attention unit end: no store drain before the slot-release barrier
# baseline (speedup 1.0000x reference)
; __device__ __forceinline__ int hw_lane() { int l; asm volatile("v_mbcnt_lo_u32_b32 %0, -1, 0\n\tv_mbcnt_hi_u32_b32 %0, -1, %0" : "=v"(l)); return l; }
; #define ATT_SBAR() __builtin_amdgcn_sched_barrier(0)
; __device__ __forceinline__ int crow(int r, int hi) { return (r & 3) + 8 * (r >> 2) + 4 * hi; }
; template <int DK, int DV, bool OFF, class QLoader> ...
;     ...
;   finishSM(pB0, pB1, l_reg, pa0, pa1, pa2, pa3); ATT_SBAR();
;   pv_all_pipe<DV>(o, vb0 + 3 * SHM_V, pa0, pa1, pa2, pa3);
;   { auto rr = __builtin_amdgcn_permlane32_swap(__float_as_uint(l_reg), __float_as_uint(l_reg), false, false);
;     const unsigned r0 = rr[0], r1 = rr[1]; l_reg = __uint_as_float(r0) + __uint_as_float(r1); }
;   const int lane_e = hw_lane(), r32e = lane_e & 31, hie = lane_e >> 5;
;   if (hie == 0) li_l[r32e] = l_reg; asm volatile("s_waitcnt lgkmcnt(0)" ::: "memory");
;   float rli[16];
; #pragma unroll
;   for (int r = 0; r < 16; ++r) rli[r] = __builtin_amdgcn_rcpf(li_l[crow(r, hie)]);
;   bf16* Ow = Ob + (long)(wid * QBLK) * ldo;
.LBB0_918:
	s_and_b32 s2, s23, 0x3fffffc0
	s_lshl_b32 s2, s2, 2
	s_add_i32 s2, s2, 0
	s_add_i32 s2, s2, 0x20000
	s_setprio 0
	v_add_f32_e32 v0, 0, v197
	v_add_f32_e32 v0, v200, v0
	v_add_f32_e32 v0, v198, v0
	v_add_f32_e32 v0, v202, v0
	v_add_f32_e32 v0, v204, v0
	v_add_f32_e32 v0, v207, v0
	v_add_f32_e32 v0, v205, v0
	v_add_f32_e32 v0, v210, v0
	v_add_f32_e32 v0, v199, v0
	v_add_f32_e32 v0, v203, v0
	v_add_f32_e32 v0, v201, v0
	v_add_f32_e32 v0, v209, v0
	v_exp_f32_e32 v74, v82
	v_add_f32_e32 v0, v206, v0
	v_exp_f32_e32 v75, v83
	v_add_f32_e32 v0, v211, v0
	v_exp_f32_e32 v76, v84
	v_add_f32_e32 v0, v208, v0
	v_exp_f32_e32 v77, v85
	v_add_f32_e32 v0, v212, v0
	v_exp_f32_e32 v78, v86
	v_add_f32_e32 v0, v0, v74
	v_exp_f32_e32 v79, v87
	v_add_f32_e32 v0, v75, v0
	v_exp_f32_e32 v80, v88
	v_add_f32_e32 v0, v76, v0
	v_exp_f32_e32 v81, v89
	v_add_f32_e32 v0, v77, v0
	v_exp_f32_e32 v82, v90
	v_add_f32_e32 v0, v78, v0
	v_exp_f32_e32 v83, v91
	v_add_f32_e32 v0, v79, v0
	v_exp_f32_e32 v84, v92
	v_add_f32_e32 v0, v80, v0
	v_exp_f32_e32 v85, v93
	v_add_f32_e32 v0, v81, v0
	v_exp_f32_e32 v86, v94
	v_add_f32_e32 v0, v82, v0
	v_exp_f32_e32 v87, v95
	v_add_f32_e32 v0, v83, v0
	v_exp_f32_e32 v88, v96
	v_add_f32_e32 v0, v84, v0
	v_exp_f32_e32 v89, v97
	v_add_f32_e32 v0, v85, v0
	v_add_f32_e32 v0, v86, v0
	v_add_f32_e32 v0, v87, v0
	v_add_f32_e32 v0, v88, v0
	v_add_f32_e32 v0, v89, v0
	v_cvt_pk_bf16_f32 v66, v197, v200
	v_cvt_pk_bf16_f32 v67, v198, v202
	v_cvt_pk_bf16_f32 v68, v204, v207
	v_cvt_pk_bf16_f32 v69, v205, v210
	v_add_f32_e32 v0, v172, v0
	v_permlane32_swap_b32_e32 v66, v68
	v_permlane32_swap_b32_e32 v67, v69
	v_cvt_pk_bf16_f32 v70, v199, v203
	v_cvt_pk_bf16_f32 v71, v201, v209
	v_cvt_pk_bf16_f32 v72, v206, v211
	v_cvt_pk_bf16_f32 v73, v208, v212
	v_cvt_pk_bf16_f32 v74, v74, v75
	v_cvt_pk_bf16_f32 v75, v76, v77
	v_cvt_pk_bf16_f32 v76, v78, v79
	v_cvt_pk_bf16_f32 v77, v80, v81
	v_cvt_pk_bf16_f32 v78, v82, v83
	v_cvt_pk_bf16_f32 v79, v84, v85
	v_cvt_pk_bf16_f32 v80, v86, v87
	v_cvt_pk_bf16_f32 v81, v88, v89
	s_nop 0
	v_permlane32_swap_b32_e32 v70, v72
	v_permlane32_swap_b32_e32 v71, v73
	v_permlane32_swap_b32_e32 v74, v76
	v_permlane32_swap_b32_e32 v75, v77
	v_permlane32_swap_b32_e32 v78, v80
	v_permlane32_swap_b32_e32 v79, v81
	ds_read_b64_tr_b16 v[82:83], v160 offset:0
	ds_read_b64_tr_b16 v[84:85], v160 offset:0x800
	ds_read_b64_tr_b16 v[86:87], v160 offset:0x1000
	ds_read_b64_tr_b16 v[88:89], v160 offset:0x1800
	ds_read_b64_tr_b16 v[90:91], v160 offset:0x2000
	ds_read_b64_tr_b16 v[92:93], v160 offset:0x2800
	ds_read_b64_tr_b16 v[94:95], v160 offset:0x3000
	ds_read_b64_tr_b16 v[96:97], v160 offset:0x3800
	ds_read_b64_tr_b16 v[98:99], v160 offset:0x200
	ds_read_b64_tr_b16 v[100:101], v160 offset:0xa00
	ds_read_b64_tr_b16 v[102:103], v160 offset:0x1200
	ds_read_b64_tr_b16 v[104:105], v160 offset:0x1a00
	ds_read_b64_tr_b16 v[106:107], v160 offset:0x2200
	ds_read_b64_tr_b16 v[108:109], v160 offset:0x2a00
	ds_read_b64_tr_b16 v[110:111], v160 offset:0x3200
	ds_read_b64_tr_b16 v[112:113], v160 offset:0x3a00
	s_nop 0
	s_waitcnt lgkmcnt(8)
	s_nop 0
	v_mfma_f32_32x32x16_bf16 v[2:17], v[66:69], v[82:85], v[2:17]
	ds_read_b64_tr_b16 v[82:83], v160 offset:0x400
	ds_read_b64_tr_b16 v[84:85], v160 offset:0xc00
	v_mfma_f32_32x32x16_bf16 v[2:17], v[70:73], v[86:89], v[2:17]
	ds_read_b64_tr_b16 v[86:87], v160 offset:0x1400
	ds_read_b64_tr_b16 v[88:89], v160 offset:0x1c00
	v_mfma_f32_32x32x16_bf16 v[2:17], v[74:77], v[90:93], v[2:17]
	ds_read_b64_tr_b16 v[90:91], v160 offset:0x2400
	ds_read_b64_tr_b16 v[92:93], v160 offset:0x2c00
	v_mfma_f32_32x32x16_bf16 v[2:17], v[78:81], v[94:97], v[2:17]
	ds_read_b64_tr_b16 v[94:95], v160 offset:0x3400
	ds_read_b64_tr_b16 v[96:97], v160 offset:0x3c00
	s_waitcnt lgkmcnt(8)
	s_nop 0
	v_mfma_f32_32x32x16_bf16 v[50:65], v[66:69], v[98:101], v[50:65]
	ds_read_b64_tr_b16 v[98:99], v160 offset:0x600
	ds_read_b64_tr_b16 v[100:101], v160 offset:0xe00
	v_mfma_f32_32x32x16_bf16 v[50:65], v[70:73], v[102:105], v[50:65]
	ds_read_b64_tr_b16 v[102:103], v160 offset:0x1600
	ds_read_b64_tr_b16 v[104:105], v160 offset:0x1e00
	v_mfma_f32_32x32x16_bf16 v[50:65], v[74:77], v[106:109], v[50:65]
	ds_read_b64_tr_b16 v[106:107], v160 offset:0x2600
	ds_read_b64_tr_b16 v[108:109], v160 offset:0x2e00
	v_mfma_f32_32x32x16_bf16 v[50:65], v[78:81], v[110:113], v[50:65]
	ds_read_b64_tr_b16 v[110:111], v160 offset:0x3600
	ds_read_b64_tr_b16 v[112:113], v160 offset:0x3e00
	s_waitcnt lgkmcnt(8)
	s_nop 0
	s_waitcnt lgkmcnt(0)
	v_mfma_f32_32x32x16_bf16 v[34:49], v[66:69], v[82:85], v[34:49]
	v_mfma_f32_32x32x16_bf16 v[18:33], v[66:69], v[98:101], v[18:33]
	v_mov_b32_e32 v68, v0
	s_nop 1
	v_permlane32_swap_b32_e32 v0, v68
	v_mbcnt_lo_u32_b32 v67, -1, 0
	v_mbcnt_hi_u32_b32 v67, -1, v67
	s_nop 0
	v_and_b32_e32 v66, 31, v67
	v_cmp_gt_u32_e32 vcc, 32, v67
	v_mfma_f32_32x32x16_bf16 v[34:49], v[70:73], v[86:89], v[34:49]
	v_mfma_f32_32x32x16_bf16 v[18:33], v[70:73], v[102:105], v[18:33]
	v_mfma_f32_32x32x16_bf16 v[34:49], v[74:77], v[90:93], v[34:49]
	v_mfma_f32_32x32x16_bf16 v[18:33], v[74:77], v[106:109], v[18:33]
	v_mfma_f32_32x32x16_bf16 v[34:49], v[78:81], v[94:97], v[34:49]
	v_mfma_f32_32x32x16_bf16 v[18:33], v[78:81], v[110:113], v[18:33]
	s_and_saveexec_b64 s[24:25], vcc
	v_lshl_add_u32 v69, v66, 2, s2
	v_add_f32_e32 v0, v0, v68
	ds_write_b32 v69, v0
	s_or_b64 exec, exec, s[24:25]
	v_ashrrev_i32_e32 v0, 3, v67
	v_and_b32_e32 v76, -4, v0
	s_waitcnt lgkmcnt(0)
	v_lshl_add_u32 v67, v76, 2, s2
	ds_read_b96 v[68:70], v67
	ds_read_b96 v[72:74], v67 offset:32
	v_or_b32_e32 v82, 3, v0
	v_lshl_add_u32 v0, v82, 2, s2
	s_ashr_i32 s23, s22, 31
	s_waitcnt lgkmcnt(0)
; __device__ __forceinline__ unsigned f2bf(float f) { unsigned u = __builtin_bit_cast(unsigned, f); return (u + 0x7fffu + ((u >> 16) & 1u)) >> 16; }
; __device__ __forceinline__ int crow(int r, int hi) { return (r & 3) + 8 * (r >> 2) + 4 * hi; }
; template <int DK, int DV, bool OFF, class QLoader> ...
;     ...
;   for (int r = 0; r < 16; ++r) rli[r] = __builtin_amdgcn_rcpf(li_l[crow(r, hie)]);
;   bf16* Ow = Ob + (long)(wid * QBLK) * ldo;
; #pragma unroll
;   for (int r = 0; r < 16; ++r) { const int orow = crow(r, hie);
; #pragma unroll
;     for (int d0 = 0; d0 < ND; ++d0) Ow[(long)orow * ldo + d0 * 32 + r32e] = (bf16)f2bf(o[d0][r] * rli[r]); }
	v_rcp_f32_e32 v75, v68
	v_rcp_f32_e32 v84, v69
	ds_read2_b32 v[68:69], v0 offset1:8
	v_rcp_f32_e32 v85, v70
	s_lshl_b64 s[4:5], s[22:23], 12
	s_add_u32 s4, s12, s4
	s_addc_u32 s5, s13, s5
	s_waitcnt lgkmcnt(0)
	v_rcp_f32_e32 v86, v68
	v_rcp_f32_e32 v87, v69
	ds_read_b96 v[68:70], v67 offset:64
	v_ashrrev_i32_e32 v77, 31, v76
	v_or_b32_e32 v78, 1, v76
	v_ashrrev_i32_e32 v79, 31, v78
	v_or_b32_e32 v80, 2, v76
	s_waitcnt lgkmcnt(0)
	v_rcp_f32_e32 v90, v70
	ds_read2_b32 v[70:71], v0 offset0:16 offset1:24
	v_rcp_f32_e32 v88, v68
	v_rcp_f32_e32 v89, v69
	v_lshlrev_b32_e32 v0, 1, v66
	v_ashrrev_i32_e32 v81, 31, v80
	s_waitcnt lgkmcnt(0)
	v_rcp_f32_e32 v91, v70
	ds_read_b96 v[68:70], v67 offset:96
	v_lshlrev_b64 v[66:67], 12, v[76:77]
	v_rcp_f32_e32 v95, v71
	v_ashrrev_i32_e32 v83, 31, v82
	v_rcp_f32_e32 v72, v72
	s_waitcnt lgkmcnt(0)
	v_rcp_f32_e32 v92, v68
	v_rcp_f32_e32 v93, v69
	v_lshl_add_u64 v[68:69], s[4:5], 0, v[0:1]
	v_mul_f32_e32 v0, v2, v75
	v_bfe_u32 v2, v0, 16, 1
	v_lshl_add_u64 v[66:67], v[68:69], 0, v[66:67]
	v_add3_u32 v0, v0, v2, s33
	global_store_short_d16_hi v[66:67], v0, off
	v_mul_f32_e32 v0, v50, v75
	v_bfe_u32 v2, v0, 16, 1
	v_add3_u32 v0, v0, v2, s33
	global_store_short_d16_hi v[66:67], v0, off offset:64
	v_mul_f32_e32 v0, v34, v75
	v_bfe_u32 v2, v0, 16, 1
	v_add3_u32 v0, v0, v2, s33
	global_store_short_d16_hi v[66:67], v0, off offset:128
	v_mul_f32_e32 v0, v18, v75
	v_bfe_u32 v2, v0, 16, 1
	v_add3_u32 v0, v0, v2, s33
	global_store_short_d16_hi v[66:67], v0, off offset:192
	v_mul_f32_e32 v0, v3, v84
	v_rcp_f32_e32 v94, v70
	v_lshlrev_b64 v[70:71], 12, v[78:79]
	v_bfe_u32 v2, v0, 16, 1
	v_lshl_add_u64 v[70:71], v[68:69], 0, v[70:71]
	v_add3_u32 v0, v0, v2, s33
	global_store_short_d16_hi v[70:71], v0, off
	v_mul_f32_e32 v0, v51, v84
	v_bfe_u32 v2, v0, 16, 1
	v_add3_u32 v0, v0, v2, s33
	global_store_short_d16_hi v[70:71], v0, off offset:64
	v_mul_f32_e32 v0, v35, v84
	v_bfe_u32 v2, v0, 16, 1
	v_add3_u32 v0, v0, v2, s33
	global_store_short_d16_hi v[70:71], v0, off offset:128
	v_mul_f32_e32 v0, v19, v84
	v_bfe_u32 v2, v0, 16, 1
	v_add3_u32 v0, v0, v2, s33
	global_store_short_d16_hi v[70:71], v0, off offset:192
	v_mul_f32_e32 v0, v4, v85
	v_lshlrev_b64 v[2:3], 12, v[80:81]
	v_bfe_u32 v4, v0, 16, 1
	v_lshl_add_u64 v[2:3], v[68:69], 0, v[2:3]
	v_add3_u32 v0, v0, v4, s33
	global_store_short_d16_hi v[2:3], v0, off
	v_mul_f32_e32 v0, v52, v85
	v_bfe_u32 v4, v0, 16, 1
	v_add3_u32 v0, v0, v4, s33
	global_store_short_d16_hi v[2:3], v0, off offset:64
	v_mul_f32_e32 v0, v36, v85
	v_bfe_u32 v4, v0, 16, 1
	v_add3_u32 v0, v0, v4, s33
	global_store_short_d16_hi v[2:3], v0, off offset:128
	v_mul_f32_e32 v0, v20, v85
	v_bfe_u32 v4, v0, 16, 1
	v_add3_u32 v0, v0, v4, s33
	global_store_short_d16_hi v[2:3], v0, off offset:192
	v_mul_f32_e32 v0, v5, v86
	v_lshlrev_b64 v[2:3], 12, v[82:83]
	v_bfe_u32 v4, v0, 16, 1
	v_lshl_add_u64 v[2:3], v[68:69], 0, v[2:3]
	v_add3_u32 v0, v0, v4, s33
	global_store_short_d16_hi v[2:3], v0, off
	v_mul_f32_e32 v0, v53, v86
	v_bfe_u32 v4, v0, 16, 1
	v_add3_u32 v0, v0, v4, s33
	global_store_short_d16_hi v[2:3], v0, off offset:64
	v_mul_f32_e32 v0, v37, v86
	v_bfe_u32 v4, v0, 16, 1
	v_add3_u32 v0, v0, v4, s33
	global_store_short_d16_hi v[2:3], v0, off offset:128
	v_mul_f32_e32 v0, v21, v86
	v_bfe_u32 v4, v0, 16, 1
	v_add3_u32 v0, v0, v4, s33
	global_store_short_d16_hi v[2:3], v0, off offset:192
	v_mul_f32_e32 v0, v6, v72
	s_mov_b32 s2, 0x9000
	v_bfe_u32 v6, v0, 16, 1
	v_add_co_u32_e32 v18, vcc, s2, v66
	v_add3_u32 v0, v0, v6, s33
	s_nop 0
	v_addc_co_u32_e32 v19, vcc, 0, v67, vcc
	global_store_short_d16_hi v[18:19], v0, off offset:-4096
	v_mul_f32_e32 v0, v54, v72
	s_mov_b64 s[4:5], 0x8000
	v_bfe_u32 v6, v0, 16, 1
	v_lshl_add_u64 v[4:5], v[66:67], 0, s[4:5]
	v_add3_u32 v0, v0, v6, s33
	global_store_short_d16_hi v[4:5], v0, off offset:64
	v_mul_f32_e32 v0, v38, v72
	v_bfe_u32 v6, v0, 16, 1
	v_rcp_f32_e32 v73, v73
	v_add3_u32 v0, v0, v6, s33
	global_store_short_d16_hi v[4:5], v0, off offset:128
	v_mul_f32_e32 v0, v22, v72
	v_bfe_u32 v6, v0, 16, 1
	v_add3_u32 v0, v0, v6, s33
	global_store_short_d16_hi v[4:5], v0, off offset:192
	v_mul_f32_e32 v0, v7, v73
	v_bfe_u32 v6, v0, 16, 1
	v_add3_u32 v0, v0, v6, s33
	global_store_short_d16_hi v[18:19], v0, off
	v_mul_f32_e32 v0, v55, v73
	s_mov_b64 s[22:23], 0x9000
	v_bfe_u32 v6, v0, 16, 1
	v_lshl_add_u64 v[4:5], v[66:67], 0, s[22:23]
	v_add3_u32 v0, v0, v6, s33
	global_store_short_d16_hi v[4:5], v0, off offset:64
	v_mul_f32_e32 v0, v39, v73
	v_bfe_u32 v6, v0, 16, 1
	v_rcp_f32_e32 v74, v74
	v_add3_u32 v0, v0, v6, s33
	global_store_short_d16_hi v[4:5], v0, off offset:128
	v_mul_f32_e32 v0, v23, v73
	v_bfe_u32 v6, v0, 16, 1
	v_add3_u32 v0, v0, v6, s33
	global_store_short_d16_hi v[4:5], v0, off offset:192
	v_mul_f32_e32 v0, v8, v74
	v_bfe_u32 v6, v0, 16, 1
	s_mov_b32 s2, 0xa000
	v_add3_u32 v0, v0, v6, s33
	v_add_co_u32_e32 v6, vcc, s2, v66
	s_mov_b64 s[22:23], 0xa000
	s_nop 0
	v_addc_co_u32_e32 v7, vcc, 0, v67, vcc
	global_store_short_d16_hi v[6:7], v0, off
	v_mul_f32_e32 v0, v56, v74
	v_bfe_u32 v6, v0, 16, 1
	v_lshl_add_u64 v[4:5], v[66:67], 0, s[22:23]
	v_add3_u32 v0, v0, v6, s33
	global_store_short_d16_hi v[4:5], v0, off offset:64
	v_mul_f32_e32 v0, v40, v74
	v_bfe_u32 v6, v0, 16, 1
	v_add3_u32 v0, v0, v6, s33
	global_store_short_d16_hi v[4:5], v0, off offset:128
	v_mul_f32_e32 v0, v24, v74
	v_bfe_u32 v6, v0, 16, 1
	v_add3_u32 v0, v0, v6, s33
	global_store_short_d16_hi v[4:5], v0, off offset:192
	v_mul_f32_e32 v0, v9, v87
	v_bfe_u32 v6, v0, 16, 1
	s_mov_b32 s2, 0x8000
	v_add3_u32 v0, v0, v6, s33
	v_add_co_u32_e32 v6, vcc, s2, v2
	v_lshl_add_u64 v[4:5], v[2:3], 0, s[4:5]
	s_nop 0
; __device__ __forceinline__ unsigned f2bf(float f) { unsigned u = __builtin_bit_cast(unsigned, f); return (u + 0x7fffu + ((u >> 16) & 1u)) >> 16; }
; __device__ __forceinline__ int crow(int r, int hi) { return (r & 3) + 8 * (r >> 2) + 4 * hi; }
; template <int DK, int DV, bool OFF, class QLoader> ...
;     ...
;   for (int r = 0; r < 16; ++r) rli[r] = __builtin_amdgcn_rcpf(li_l[crow(r, hie)]);
;   bf16* Ow = Ob + (long)(wid * QBLK) * ldo;
; #pragma unroll
;   for (int r = 0; r < 16; ++r) { const int orow = crow(r, hie);
; #pragma unroll
;     for (int d0 = 0; d0 < ND; ++d0) Ow[(long)orow * ldo + d0 * 32 + r32e] = (bf16)f2bf(o[d0][r] * rli[r]); }
;   __syncthreads();
	v_addc_co_u32_e32 v7, vcc, 0, v3, vcc
	global_store_short_d16_hi v[6:7], v0, off
	v_mul_f32_e32 v0, v57, v87
	v_bfe_u32 v6, v0, 16, 1
	v_add3_u32 v0, v0, v6, s33
	global_store_short_d16_hi v[4:5], v0, off offset:64
	v_mul_f32_e32 v0, v41, v87
	v_bfe_u32 v6, v0, 16, 1
	v_add3_u32 v0, v0, v6, s33
	global_store_short_d16_hi v[4:5], v0, off offset:128
	v_mul_f32_e32 v0, v25, v87
	v_bfe_u32 v6, v0, 16, 1
	v_add3_u32 v0, v0, v6, s33
	global_store_short_d16_hi v[4:5], v0, off offset:192
	v_mul_f32_e32 v0, v10, v88
	v_bfe_u32 v6, v0, 16, 1
	s_mov_b32 s2, 0x11000
	v_add3_u32 v0, v0, v6, s33
	v_add_co_u32_e32 v6, vcc, s2, v66
	s_mov_b64 s[22:23], 0x10000
	s_nop 0
	v_addc_co_u32_e32 v7, vcc, 0, v67, vcc
	global_store_short_d16_hi v[6:7], v0, off offset:-4096
	v_mul_f32_e32 v0, v58, v88
	v_bfe_u32 v8, v0, 16, 1
	v_lshl_add_u64 v[4:5], v[66:67], 0, s[22:23]
	v_add3_u32 v0, v0, v8, s33
	global_store_short_d16_hi v[4:5], v0, off offset:64
	v_mul_f32_e32 v0, v42, v88
	v_bfe_u32 v8, v0, 16, 1
	v_add3_u32 v0, v0, v8, s33
	global_store_short_d16_hi v[4:5], v0, off offset:128
	v_mul_f32_e32 v0, v26, v88
	v_bfe_u32 v8, v0, 16, 1
	v_add3_u32 v0, v0, v8, s33
	global_store_short_d16_hi v[4:5], v0, off offset:192
	v_mul_f32_e32 v0, v11, v89
	v_bfe_u32 v8, v0, 16, 1
	v_add3_u32 v0, v0, v8, s33
	global_store_short_d16_hi v[6:7], v0, off
	v_mul_f32_e32 v0, v59, v89
	s_mov_b64 s[4:5], 0x11000
	v_bfe_u32 v6, v0, 16, 1
	v_lshl_add_u64 v[4:5], v[66:67], 0, s[4:5]
	v_add3_u32 v0, v0, v6, s33
	global_store_short_d16_hi v[4:5], v0, off offset:64
	v_mul_f32_e32 v0, v43, v89
	v_bfe_u32 v6, v0, 16, 1
	v_add3_u32 v0, v0, v6, s33
	global_store_short_d16_hi v[4:5], v0, off offset:128
	v_mul_f32_e32 v0, v27, v89
	v_bfe_u32 v6, v0, 16, 1
	v_add3_u32 v0, v0, v6, s33
	global_store_short_d16_hi v[4:5], v0, off offset:192
	v_mul_f32_e32 v0, v12, v90
	v_bfe_u32 v6, v0, 16, 1
	s_mov_b32 s2, 0x12000
	v_add3_u32 v0, v0, v6, s33
	v_add_co_u32_e32 v6, vcc, s2, v66
	s_mov_b64 s[4:5], 0x12000
	s_nop 0
	v_addc_co_u32_e32 v7, vcc, 0, v67, vcc
	global_store_short_d16_hi v[6:7], v0, off
	v_mul_f32_e32 v0, v60, v90
	v_bfe_u32 v6, v0, 16, 1
	v_lshl_add_u64 v[4:5], v[66:67], 0, s[4:5]
	v_add3_u32 v0, v0, v6, s33
	global_store_short_d16_hi v[4:5], v0, off offset:64
	v_mul_f32_e32 v0, v44, v90
	v_bfe_u32 v6, v0, 16, 1
	v_add3_u32 v0, v0, v6, s33
	global_store_short_d16_hi v[4:5], v0, off offset:128
	v_mul_f32_e32 v0, v28, v90
	v_bfe_u32 v6, v0, 16, 1
	v_add3_u32 v0, v0, v6, s33
	global_store_short_d16_hi v[4:5], v0, off offset:192
	v_mul_f32_e32 v0, v13, v91
	v_bfe_u32 v6, v0, 16, 1
	s_mov_b32 s2, 0x10000
	v_add3_u32 v0, v0, v6, s33
	v_add_co_u32_e32 v6, vcc, s2, v2
	v_lshl_add_u64 v[4:5], v[2:3], 0, s[22:23]
	s_nop 0
	v_addc_co_u32_e32 v7, vcc, 0, v3, vcc
	global_store_short_d16_hi v[6:7], v0, off
	v_mul_f32_e32 v0, v61, v91
	v_bfe_u32 v6, v0, 16, 1
	v_add3_u32 v0, v0, v6, s33
	global_store_short_d16_hi v[4:5], v0, off offset:64
	v_mul_f32_e32 v0, v45, v91
	v_bfe_u32 v6, v0, 16, 1
	v_add3_u32 v0, v0, v6, s33
	global_store_short_d16_hi v[4:5], v0, off offset:128
	v_mul_f32_e32 v0, v29, v91
	v_bfe_u32 v6, v0, 16, 1
	v_add3_u32 v0, v0, v6, s33
	global_store_short_d16_hi v[4:5], v0, off offset:192
	v_mul_f32_e32 v0, v14, v92
	v_bfe_u32 v6, v0, 16, 1
	s_mov_b32 s2, 0x19000
	v_add3_u32 v0, v0, v6, s33
	v_add_co_u32_e32 v6, vcc, s2, v66
	s_mov_b64 s[22:23], 0x18000
	s_nop 0
	v_addc_co_u32_e32 v7, vcc, 0, v67, vcc
	global_store_short_d16_hi v[6:7], v0, off offset:-4096
	v_mul_f32_e32 v0, v62, v92
	v_bfe_u32 v8, v0, 16, 1
	v_lshl_add_u64 v[4:5], v[66:67], 0, s[22:23]
	v_add3_u32 v0, v0, v8, s33
	global_store_short_d16_hi v[4:5], v0, off offset:64
	v_mul_f32_e32 v0, v46, v92
	v_bfe_u32 v8, v0, 16, 1
	v_add3_u32 v0, v0, v8, s33
	global_store_short_d16_hi v[4:5], v0, off offset:128
	v_mul_f32_e32 v0, v30, v92
	v_bfe_u32 v8, v0, 16, 1
	v_add3_u32 v0, v0, v8, s33
	global_store_short_d16_hi v[4:5], v0, off offset:192
	v_mul_f32_e32 v0, v15, v93
	v_bfe_u32 v8, v0, 16, 1
	v_add3_u32 v0, v0, v8, s33
	global_store_short_d16_hi v[6:7], v0, off
	v_mul_f32_e32 v0, v63, v93
	s_mov_b64 s[4:5], 0x19000
	v_bfe_u32 v6, v0, 16, 1
	v_lshl_add_u64 v[4:5], v[66:67], 0, s[4:5]
	v_add3_u32 v0, v0, v6, s33
	global_store_short_d16_hi v[4:5], v0, off offset:64
	v_mul_f32_e32 v0, v47, v93
	v_bfe_u32 v6, v0, 16, 1
	v_add3_u32 v0, v0, v6, s33
	global_store_short_d16_hi v[4:5], v0, off offset:128
	v_mul_f32_e32 v0, v31, v93
	v_bfe_u32 v6, v0, 16, 1
	v_add3_u32 v0, v0, v6, s33
	global_store_short_d16_hi v[4:5], v0, off offset:192
	v_mul_f32_e32 v0, v16, v94
	v_bfe_u32 v6, v0, 16, 1
	s_mov_b32 s2, 0x1a000
	v_add3_u32 v0, v0, v6, s33
	v_add_co_u32_e32 v6, vcc, s2, v66
	s_mov_b64 s[4:5], 0x1a000
	s_nop 0
	v_addc_co_u32_e32 v7, vcc, 0, v67, vcc
	global_store_short_d16_hi v[6:7], v0, off
	v_mul_f32_e32 v0, v64, v94
	v_bfe_u32 v6, v0, 16, 1
	v_lshl_add_u64 v[4:5], v[66:67], 0, s[4:5]
	v_add3_u32 v0, v0, v6, s33
	global_store_short_d16_hi v[4:5], v0, off offset:64
	v_mul_f32_e32 v0, v48, v94
	v_bfe_u32 v6, v0, 16, 1
	v_add3_u32 v0, v0, v6, s33
	global_store_short_d16_hi v[4:5], v0, off offset:128
	v_mul_f32_e32 v0, v32, v94
	v_bfe_u32 v6, v0, 16, 1
	v_add3_u32 v0, v0, v6, s33
	global_store_short_d16_hi v[4:5], v0, off offset:192
	v_mul_f32_e32 v0, v17, v95
	s_mov_b32 s2, 0x18000
	v_lshl_add_u64 v[4:5], v[2:3], 0, s[22:23]
	v_bfe_u32 v6, v0, 16, 1
	v_add_co_u32_e32 v2, vcc, s2, v2
	v_add3_u32 v0, v0, v6, s33
	s_nop 0
	v_addc_co_u32_e32 v3, vcc, 0, v3, vcc
	global_store_short_d16_hi v[2:3], v0, off
	v_mul_f32_e32 v0, v65, v95
	v_bfe_u32 v2, v0, 16, 1
	v_add3_u32 v0, v0, v2, s33
	global_store_short_d16_hi v[4:5], v0, off offset:64
	v_mul_f32_e32 v0, v49, v95
	v_bfe_u32 v2, v0, 16, 1
	v_add3_u32 v0, v0, v2, s33
	global_store_short_d16_hi v[4:5], v0, off offset:128
	v_mul_f32_e32 v0, v33, v95
	v_bfe_u32 v2, v0, 16, 1
	v_add3_u32 v0, v0, v2, s33
	global_store_short_d16_hi v[4:5], v0, off offset:192
	s_barrier

; __device__ __forceinline__ int hw_lane() { int l; asm volatile("v_mbcnt_lo_u32_b32 %0, -1, 0\n\tv_mbcnt_hi_u32_b32 %0, -1, %0" : "=v"(l)); return l; }
; #define ATT_SBAR() __builtin_amdgcn_sched_barrier(0)
; __device__ __forceinline__ int crow(int r, int hi) { return (r & 3) + 8 * (r >> 2) + 4 * hi; }
; template <int DK, int DV, bool OFF, class QLoader> ...
;     ...
;   finishSM(pB0, pB1, l_reg, pa0, pa1, pa2, pa3); ATT_SBAR();
;   pv_all_pipe<DV>(o, vb0 + 3 * SHM_V, pa0, pa1, pa2, pa3);
;   { auto rr = __builtin_amdgcn_permlane32_swap(__float_as_uint(l_reg), __float_as_uint(l_reg), false, false);
;     const unsigned r0 = rr[0], r1 = rr[1]; l_reg = __uint_as_float(r0) + __uint_as_float(r1); }
;   const int lane_e = hw_lane(), r32e = lane_e & 31, hie = lane_e >> 5;
;   if (hie == 0) li_l[r32e] = l_reg; asm volatile("s_waitcnt lgkmcnt(0)" ::: "memory");
;   float rli[16];
; #pragma unroll
;   for (int r = 0; r < 16; ++r) rli[r] = __builtin_amdgcn_rcpf(li_l[crow(r, hie)]);
;   bf16* Ow = Ob + (long)(wid * QBLK) * ldo;
.LBB0_1497:
	s_and_b32 s0, s31, 0x3fffffc0
	s_lshl_b32 s0, s0, 2
	s_add_i32 s31, s0, 0
	s_add_i32 s31, s31, 0x18000
	s_setprio 0
	v_add_f32_e32 v0, 0, v184
	v_add_f32_e32 v0, v186, v0
	v_add_f32_e32 v0, v185, v0
	v_add_f32_e32 v0, v187, v0
	v_add_f32_e32 v0, v189, v0
	v_add_f32_e32 v0, v193, v0
	v_add_f32_e32 v0, v192, v0
	v_add_f32_e32 v0, v194, v0
	v_add_f32_e32 v0, v188, v0
	v_add_f32_e32 v0, v191, v0
	v_add_f32_e32 v0, v190, v0
	v_add_f32_e32 v0, v196, v0
	v_exp_f32_e32 v50, v34
	v_add_f32_e32 v0, v195, v0
	v_exp_f32_e32 v51, v35
	v_add_f32_e32 v0, v198, v0
	v_exp_f32_e32 v52, v36
	v_add_f32_e32 v0, v197, v0
	v_exp_f32_e32 v53, v37
	v_add_f32_e32 v0, v199, v0
	v_exp_f32_e32 v54, v38
	v_add_f32_e32 v0, v50, v0
	v_exp_f32_e32 v55, v39
	v_add_f32_e32 v0, v51, v0
	v_exp_f32_e32 v56, v40
	v_add_f32_e32 v0, v52, v0
	v_exp_f32_e32 v57, v41
	v_add_f32_e32 v0, v53, v0
	v_exp_f32_e32 v58, v42
	v_add_f32_e32 v0, v54, v0
	v_exp_f32_e32 v59, v43
	v_add_f32_e32 v0, v55, v0
	v_exp_f32_e32 v60, v44
	v_add_f32_e32 v0, v56, v0
	v_exp_f32_e32 v61, v45
	v_add_f32_e32 v0, v57, v0
	v_exp_f32_e32 v62, v46
	v_add_f32_e32 v0, v58, v0
	v_exp_f32_e32 v63, v47
	v_add_f32_e32 v0, v59, v0
	v_exp_f32_e32 v64, v48
	v_add_f32_e32 v0, v60, v0
	v_exp_f32_e32 v49, v49
	v_add_f32_e32 v0, v61, v0
	v_add_f32_e32 v0, v62, v0
	v_add_f32_e32 v0, v63, v0
	v_add_f32_e32 v0, v64, v0
	v_add_f32_e32 v0, v49, v0
	v_cvt_pk_bf16_f32 v34, v184, v186
	v_cvt_pk_bf16_f32 v35, v185, v187
	v_cvt_pk_bf16_f32 v36, v189, v193
	v_cvt_pk_bf16_f32 v37, v192, v194
	v_add_f32_e32 v0, v145, v0
	v_permlane32_swap_b32_e32 v34, v36
	v_permlane32_swap_b32_e32 v35, v37
	v_cvt_pk_bf16_f32 v38, v188, v191
	v_cvt_pk_bf16_f32 v39, v190, v196
	v_cvt_pk_bf16_f32 v40, v195, v198
	v_cvt_pk_bf16_f32 v41, v197, v199
	v_cvt_pk_bf16_f32 v42, v50, v51
	v_cvt_pk_bf16_f32 v43, v52, v53
	v_cvt_pk_bf16_f32 v44, v54, v55
	v_cvt_pk_bf16_f32 v45, v56, v57
	v_cvt_pk_bf16_f32 v46, v58, v59
	v_cvt_pk_bf16_f32 v47, v60, v61
	v_cvt_pk_bf16_f32 v48, v62, v63
	v_cvt_pk_bf16_f32 v49, v64, v49
	s_nop 0
	v_permlane32_swap_b32_e32 v38, v40
	v_permlane32_swap_b32_e32 v39, v41
	v_permlane32_swap_b32_e32 v42, v44
	v_permlane32_swap_b32_e32 v43, v45
	v_permlane32_swap_b32_e32 v46, v48
	v_permlane32_swap_b32_e32 v47, v49
	ds_read_b64_tr_b16 v[50:51], v96 offset:0
	ds_read_b64_tr_b16 v[52:53], v96 offset:0x400
	ds_read_b64_tr_b16 v[54:55], v96 offset:0x800
	ds_read_b64_tr_b16 v[56:57], v96 offset:0xc00
	ds_read_b64_tr_b16 v[58:59], v96 offset:0x1000
	ds_read_b64_tr_b16 v[60:61], v96 offset:0x1400
	ds_read_b64_tr_b16 v[62:63], v96 offset:0x1800
	ds_read_b64_tr_b16 v[64:65], v96 offset:0x1c00
	ds_read_b64_tr_b16 v[66:67], v96 offset:0x200
	ds_read_b64_tr_b16 v[68:69], v96 offset:0x600
	ds_read_b64_tr_b16 v[70:71], v96 offset:0xa00
	ds_read_b64_tr_b16 v[72:73], v96 offset:0xe00
	ds_read_b64_tr_b16 v[74:75], v96 offset:0x1200
	ds_read_b64_tr_b16 v[76:77], v96 offset:0x1600
	ds_read_b64_tr_b16 v[78:79], v96 offset:0x1a00
	ds_read_b64_tr_b16 v[80:81], v96 offset:0x1e00
	s_nop 0
	s_waitcnt lgkmcnt(8)
	s_nop 0
	v_mfma_f32_32x32x16_bf16 v[2:17], v[34:37], v[50:53], v[2:17]
	s_waitcnt lgkmcnt(0)
	s_nop 0
	v_mfma_f32_32x32x16_bf16 v[18:33], v[34:37], v[66:69], v[18:33]
	v_mov_b32_e32 v36, v0
	s_nop 1
	v_permlane32_swap_b32_e32 v0, v36
	v_mbcnt_lo_u32_b32 v35, -1, 0
	v_mbcnt_hi_u32_b32 v35, -1, v35
	s_nop 0
	v_and_b32_e32 v34, 31, v35
	v_cmp_gt_u32_e32 vcc, 32, v35
	v_mfma_f32_32x32x16_bf16 v[2:17], v[38:41], v[54:57], v[2:17]
	v_mfma_f32_32x32x16_bf16 v[18:33], v[38:41], v[70:73], v[18:33]
	v_mfma_f32_32x32x16_bf16 v[2:17], v[42:45], v[58:61], v[2:17]
	v_mfma_f32_32x32x16_bf16 v[18:33], v[42:45], v[74:77], v[18:33]
	v_mfma_f32_32x32x16_bf16 v[2:17], v[46:49], v[62:65], v[2:17]
	v_mfma_f32_32x32x16_bf16 v[18:33], v[46:49], v[78:81], v[18:33]
	s_and_saveexec_b64 s[0:1], vcc
	v_lshl_add_u32 v37, v34, 2, s31
	v_add_f32_e32 v0, v0, v36
	ds_write_b32 v37, v0
	s_or_b64 exec, exec, s[0:1]
	v_ashrrev_i32_e32 v0, 3, v35
	v_and_b32_e32 v44, -4, v0
	s_waitcnt lgkmcnt(0)
	v_lshl_add_u32 v35, v44, 2, s31
	ds_read_b96 v[36:38], v35
	ds_read_b96 v[40:42], v35 offset:32
	v_or_b32_e32 v50, 3, v0
	v_lshl_add_u32 v0, v50, 2, s31
	s_ashr_i32 s31, s30, 31
	s_waitcnt lgkmcnt(0)
	v_rcp_f32_e32 v43, v36
	v_rcp_f32_e32 v52, v37
	ds_read2_b32 v[36:37], v0 offset1:8
	v_rcp_f32_e32 v53, v38
	s_lshl_b64 s[0:1], s[30:31], 11
	s_add_u32 s0, s16, s0
	s_addc_u32 s1, s17, s1
	s_waitcnt lgkmcnt(0)
	v_rcp_f32_e32 v54, v36
	v_rcp_f32_e32 v55, v37
	ds_read_b96 v[36:38], v35 offset:64
	v_ashrrev_i32_e32 v45, 31, v44
	v_or_b32_e32 v46, 1, v44
	v_ashrrev_i32_e32 v47, 31, v46
	v_or_b32_e32 v48, 2, v44
	s_waitcnt lgkmcnt(0)
	v_rcp_f32_e32 v58, v38
	ds_read2_b32 v[38:39], v0 offset0:16 offset1:24
	v_rcp_f32_e32 v56, v36
	v_rcp_f32_e32 v57, v37
	v_lshlrev_b32_e32 v0, 1, v34
	v_ashrrev_i32_e32 v49, 31, v48
	s_waitcnt lgkmcnt(0)
	v_rcp_f32_e32 v59, v38
	ds_read_b96 v[36:38], v35 offset:96
	v_lshl_add_u64 v[34:35], s[0:1], 0, v[0:1]
	v_mul_f32_e32 v0, v2, v43
	v_bfe_u32 v2, v0, 16, 1
	v_add3_u32 v0, v0, v2, s33
	s_waitcnt lgkmcnt(0)
; __device__ __forceinline__ unsigned f2bf(float f) { unsigned u = __builtin_bit_cast(unsigned, f); return (u + 0x7fffu + ((u >> 16) & 1u)) >> 16; }
; __device__ __forceinline__ int crow(int r, int hi) { return (r & 3) + 8 * (r >> 2) + 4 * hi; }
; template <int DK, int DV, bool OFF, class QLoader> ...
;     ...
;   for (int r = 0; r < 16; ++r) rli[r] = __builtin_amdgcn_rcpf(li_l[crow(r, hie)]);
;   bf16* Ow = Ob + (long)(wid * QBLK) * ldo;
; #pragma unroll
;   for (int r = 0; r < 16; ++r) { const int orow = crow(r, hie);
; #pragma unroll
;     for (int d0 = 0; d0 < ND; ++d0) Ow[(long)orow * ldo + d0 * 32 + r32e] = (bf16)f2bf(o[d0][r] * rli[r]); }
;   __syncthreads();
	v_rcp_f32_e32 v60, v36
	v_rcp_f32_e32 v61, v37
	v_lshlrev_b64 v[36:37], 11, v[44:45]
	v_lshl_add_u64 v[36:37], v[34:35], 0, v[36:37]
	global_store_short_d16_hi v[36:37], v0, off
	v_mul_f32_e32 v0, v18, v43
	v_bfe_u32 v2, v0, 16, 1
	v_add3_u32 v0, v0, v2, s33
	global_store_short_d16_hi v[36:37], v0, off offset:64
	v_mul_f32_e32 v0, v3, v52
	v_rcp_f32_e32 v62, v38
	v_rcp_f32_e32 v63, v39
	v_lshlrev_b64 v[38:39], 11, v[46:47]
	v_bfe_u32 v2, v0, 16, 1
	v_lshl_add_u64 v[38:39], v[34:35], 0, v[38:39]
	v_add3_u32 v0, v0, v2, s33
	global_store_short_d16_hi v[38:39], v0, off
	v_mul_f32_e32 v0, v19, v52
	v_bfe_u32 v2, v0, 16, 1
	v_add3_u32 v0, v0, v2, s33
	global_store_short_d16_hi v[38:39], v0, off offset:64
	v_mul_f32_e32 v0, v4, v53
	v_lshlrev_b64 v[2:3], 11, v[48:49]
	v_bfe_u32 v4, v0, 16, 1
	v_lshl_add_u64 v[2:3], v[34:35], 0, v[2:3]
	v_add3_u32 v0, v0, v4, s33
	global_store_short_d16_hi v[2:3], v0, off
	v_mul_f32_e32 v0, v20, v53
	v_bfe_u32 v4, v0, 16, 1
	v_add3_u32 v0, v0, v4, s33
	v_ashrrev_i32_e32 v51, 31, v50
	global_store_short_d16_hi v[2:3], v0, off offset:64
	v_mul_f32_e32 v0, v5, v54
	v_lshlrev_b64 v[2:3], 11, v[50:51]
	v_bfe_u32 v4, v0, 16, 1
	v_rcp_f32_e32 v40, v40
	v_lshl_add_u64 v[2:3], v[34:35], 0, v[2:3]
	v_add3_u32 v0, v0, v4, s33
	global_store_short_d16_hi v[2:3], v0, off
	v_mul_f32_e32 v0, v21, v54
	v_bfe_u32 v4, v0, 16, 1
	s_movk_i32 s30, 0x4000
	v_add3_u32 v0, v0, v4, s33
	v_add_co_u32_e32 v18, vcc, s30, v36
	global_store_short_d16_hi v[2:3], v0, off offset:64
	v_mul_f32_e32 v0, v6, v40
	v_addc_co_u32_e32 v19, vcc, 0, v37, vcc
	s_movk_i32 s0, 0x5000
	v_bfe_u32 v6, v0, 16, 1
	v_add_co_u32_e32 v20, vcc, s0, v36
	v_rcp_f32_e32 v41, v41
	v_add3_u32 v0, v0, v6, s33
	v_addc_co_u32_e32 v21, vcc, 0, v37, vcc
	global_store_short_d16_hi v[20:21], v0, off offset:-4096
	v_mul_f32_e32 v0, v22, v40
	s_mov_b64 s[38:39], 0x4000
	v_bfe_u32 v6, v0, 16, 1
	v_lshl_add_u64 v[4:5], v[36:37], 0, s[38:39]
	v_add3_u32 v0, v0, v6, s33
	global_store_short_d16_hi v[4:5], v0, off offset:64
	v_mul_f32_e32 v0, v7, v41
	v_bfe_u32 v6, v0, 16, 1
	v_rcp_f32_e32 v42, v42
	v_add3_u32 v0, v0, v6, s33
	global_store_short_d16_hi v[18:19], v0, off offset:2048
	v_mul_f32_e32 v0, v23, v41
	s_mov_b64 s[0:1], 0x4800
	v_bfe_u32 v6, v0, 16, 1
	v_lshl_add_u64 v[4:5], v[36:37], 0, s[0:1]
	v_add3_u32 v0, v0, v6, s33
	global_store_short_d16_hi v[4:5], v0, off offset:64
	v_mul_f32_e32 v0, v8, v42
	v_bfe_u32 v6, v0, 16, 1
	v_add3_u32 v0, v0, v6, s33
	global_store_short_d16_hi v[20:21], v0, off
	v_mul_f32_e32 v0, v24, v42
	s_mov_b64 s[0:1], 0x5000
	v_bfe_u32 v6, v0, 16, 1
	v_lshl_add_u64 v[4:5], v[36:37], 0, s[0:1]
	v_add3_u32 v0, v0, v6, s33
	global_store_short_d16_hi v[4:5], v0, off offset:64
	v_mul_f32_e32 v0, v9, v55
	v_bfe_u32 v6, v0, 16, 1
	v_add3_u32 v0, v0, v6, s33
	v_add_co_u32_e32 v6, vcc, s30, v2
	v_lshl_add_u64 v[4:5], v[2:3], 0, s[38:39]
	s_nop 0
	v_addc_co_u32_e32 v7, vcc, 0, v3, vcc
	global_store_short_d16_hi v[6:7], v0, off
	v_mul_f32_e32 v0, v25, v55
	v_bfe_u32 v6, v0, 16, 1
	v_add3_u32 v0, v0, v6, s33
	global_store_short_d16_hi v[4:5], v0, off offset:64
	v_mul_f32_e32 v0, v10, v56
	v_bfe_u32 v6, v0, 16, 1
	s_mov_b32 s30, 0x8000
	v_add3_u32 v0, v0, v6, s33
	v_add_co_u32_e32 v6, vcc, s30, v36
	s_mov_b32 s0, 0x9000
	s_nop 0
	v_addc_co_u32_e32 v7, vcc, 0, v37, vcc
	v_add_co_u32_e32 v8, vcc, s0, v36
	s_mov_b64 s[38:39], 0x8000
	s_nop 0
	v_addc_co_u32_e32 v9, vcc, 0, v37, vcc
	global_store_short_d16_hi v[8:9], v0, off offset:-4096
	v_mul_f32_e32 v0, v26, v56
	v_bfe_u32 v10, v0, 16, 1
	v_lshl_add_u64 v[4:5], v[36:37], 0, s[38:39]
	v_add3_u32 v0, v0, v10, s33
	global_store_short_d16_hi v[4:5], v0, off offset:64
	v_mul_f32_e32 v0, v11, v57
	v_bfe_u32 v10, v0, 16, 1
	v_add3_u32 v0, v0, v10, s33
	global_store_short_d16_hi v[6:7], v0, off offset:2048
	v_mul_f32_e32 v0, v27, v57
	s_mov_b64 s[0:1], 0x8800
	v_bfe_u32 v6, v0, 16, 1
	v_lshl_add_u64 v[4:5], v[36:37], 0, s[0:1]
	v_add3_u32 v0, v0, v6, s33
	global_store_short_d16_hi v[4:5], v0, off offset:64
	v_mul_f32_e32 v0, v12, v58
	v_bfe_u32 v6, v0, 16, 1
	v_add3_u32 v0, v0, v6, s33
	global_store_short_d16_hi v[8:9], v0, off
	v_mul_f32_e32 v0, v28, v58
	s_mov_b64 s[0:1], 0x9000
	v_bfe_u32 v6, v0, 16, 1
	v_lshl_add_u64 v[4:5], v[36:37], 0, s[0:1]
	v_add3_u32 v0, v0, v6, s33
	global_store_short_d16_hi v[4:5], v0, off offset:64
	v_mul_f32_e32 v0, v13, v59
	v_bfe_u32 v6, v0, 16, 1
	v_add3_u32 v0, v0, v6, s33
	v_add_co_u32_e32 v6, vcc, s30, v2
	v_lshl_add_u64 v[4:5], v[2:3], 0, s[38:39]
	s_nop 0
	v_addc_co_u32_e32 v7, vcc, 0, v3, vcc
	global_store_short_d16_hi v[6:7], v0, off
	v_mul_f32_e32 v0, v29, v59
	v_bfe_u32 v6, v0, 16, 1
	v_add3_u32 v0, v0, v6, s33
	global_store_short_d16_hi v[4:5], v0, off offset:64
	v_mul_f32_e32 v0, v14, v60
	v_bfe_u32 v6, v0, 16, 1
	s_mov_b32 s0, 0xc000
	v_add3_u32 v0, v0, v6, s33
	v_add_co_u32_e32 v6, vcc, s0, v36
	s_mov_b64 s[30:31], 0xc000
	s_nop 0
	v_addc_co_u32_e32 v7, vcc, 0, v37, vcc
	global_store_short_d16_hi v[6:7], v0, off
	v_mul_f32_e32 v0, v30, v60
	v_bfe_u32 v8, v0, 16, 1
	v_lshl_add_u64 v[4:5], v[36:37], 0, s[30:31]
	v_add3_u32 v0, v0, v8, s33
	global_store_short_d16_hi v[4:5], v0, off offset:64
	v_mul_f32_e32 v0, v15, v61
	v_bfe_u32 v8, v0, 16, 1
	v_add3_u32 v0, v0, v8, s33
	global_store_short_d16_hi v[6:7], v0, off offset:2048
	v_mul_f32_e32 v0, v31, v61
	s_mov_b64 s[0:1], 0xc800
	v_bfe_u32 v6, v0, 16, 1
	v_lshl_add_u64 v[4:5], v[36:37], 0, s[0:1]
	v_add3_u32 v0, v0, v6, s33
	global_store_short_d16_hi v[4:5], v0, off offset:64
	v_mul_f32_e32 v0, v16, v62
	v_bfe_u32 v6, v0, 16, 1
	v_add3_u32 v0, v0, v6, s33
	v_add_co_u32_e32 v6, vcc, 0xd000, v36
	s_mov_b64 s[0:1], 0xd000
	s_nop 0
	v_addc_co_u32_e32 v7, vcc, 0, v37, vcc
	global_store_short_d16_hi v[6:7], v0, off
	v_mul_f32_e32 v0, v32, v62
	v_bfe_u32 v6, v0, 16, 1
	v_lshl_add_u64 v[4:5], v[36:37], 0, s[0:1]
	v_add3_u32 v0, v0, v6, s33
	global_store_short_d16_hi v[4:5], v0, off offset:64
	v_mul_f32_e32 v0, v17, v63
	v_lshl_add_u64 v[4:5], v[2:3], 0, s[30:31]
	v_bfe_u32 v6, v0, 16, 1
	v_add_co_u32_e32 v2, vcc, 0xc000, v2
	v_add3_u32 v0, v0, v6, s33
	s_nop 0
	v_addc_co_u32_e32 v3, vcc, 0, v3, vcc
	global_store_short_d16_hi v[2:3], v0, off
	v_mul_f32_e32 v0, v33, v63
	v_bfe_u32 v2, v0, 16, 1
	v_add3_u32 v0, v0, v2, s33
	global_store_short_d16_hi v[4:5], v0, off offset:64
	s_barrier
